# dense-up and MoE-up GEMMs: ALIGN_EPI and re-stagger barriers skipped between units (halves keep the K-loop stagger across the epilogue)
# baseline (speedup 1.0000x reference)
.LBB0_654:
	ds_read_b128 v[152:155], v147
	ds_read_b128 v[156:159], v147 offset:1024
	ds_read_b128 v[160:163], v147 offset:2048
	ds_read_b128 v[164:167], v147 offset:3072
	ds_read_b128 v[168:171], v148
	ds_read_b128 v[172:175], v148 offset:1024
	ds_read_b128 v[176:179], v148 offset:2048
	ds_read_b128 v[180:183], v148 offset:3072
	s_add_u32 s28, s26, 0xfffc0080
	s_addc_u32 s29, s27, -1
	s_cmp_eq_u32 s74, 12
	s_cselect_b32 s31, s11, s29
	s_cselect_b32 s30, s62, s28
	s_cselect_b32 s29, s21, s73
	s_cselect_b32 s28, s63, s72
	v_lshl_add_u64 v[144:145], s[26:27], 0, v[140:141]
	s_add_i32 m0, s1, 0xc000
	ds_read_b128 v[184:187], v149
	ds_read_b128 v[188:191], v149 offset:1024
	ds_read_b128 v[192:195], v149 offset:2048
	ds_read_b128 v[196:199], v149 offset:3072
	ds_read_b128 v[200:203], v149 offset:4096
	ds_read_b128 v[204:207], v149 offset:5120
	ds_read_b128 v[208:211], v149 offset:6144
	ds_read_b128 v[212:215], v149 offset:7168
	global_load_lds_dwordx4 v[144:145], off
	v_lshl_add_u64 v[144:145], s[26:27], 0, v[142:143]
	s_add_i32 m0, s1, 0xe000
	s_nop 0
	global_load_lds_dwordx4 v[144:145], off
	s_waitcnt vmcnt(8)
	s_waitcnt lgkmcnt(0)
	s_barrier
	s_setprio 1
	s_waitcnt lgkmcnt(0)
	v_mfma_f32_16x16x32_bf16 v[126:129], v[152:155], v[184:187], v[126:129]
	v_mfma_f32_16x16x32_bf16 v[122:125], v[160:163], v[184:187], v[122:125]
	v_mfma_f32_16x16x32_bf16 v[110:113], v[152:155], v[192:195], v[110:113]
	v_mfma_f32_16x16x32_bf16 v[106:109], v[160:163], v[192:195], v[106:109]
	v_mfma_f32_16x16x32_bf16 v[94:97], v[152:155], v[200:203], v[94:97]
	v_mfma_f32_16x16x32_bf16 v[90:93], v[160:163], v[200:203], v[90:93]
	v_mfma_f32_16x16x32_bf16 v[78:81], v[152:155], v[208:211], v[78:81]
	v_mfma_f32_16x16x32_bf16 v[74:77], v[160:163], v[208:211], v[74:77]
	v_mfma_f32_16x16x32_bf16 v[126:129], v[156:159], v[188:191], v[126:129]
	v_mfma_f32_16x16x32_bf16 v[122:125], v[164:167], v[188:191], v[122:125]
	v_mfma_f32_16x16x32_bf16 v[110:113], v[156:159], v[196:199], v[110:113]
	v_mfma_f32_16x16x32_bf16 v[106:109], v[164:167], v[196:199], v[106:109]
	v_mfma_f32_16x16x32_bf16 v[94:97], v[156:159], v[204:207], v[94:97]
	v_mfma_f32_16x16x32_bf16 v[90:93], v[164:167], v[204:207], v[90:93]
	v_mfma_f32_16x16x32_bf16 v[78:81], v[156:159], v[212:215], v[78:81]
	v_mfma_f32_16x16x32_bf16 v[74:77], v[164:167], v[212:215], v[74:77]
	s_setprio 0
	s_setprio 1
	v_mfma_f32_16x16x32_bf16 v[118:121], v[168:171], v[184:187], v[118:121]
	v_mfma_f32_16x16x32_bf16 v[114:117], v[176:179], v[184:187], v[114:117]
	v_mfma_f32_16x16x32_bf16 v[102:105], v[168:171], v[192:195], v[102:105]
	v_mfma_f32_16x16x32_bf16 v[98:101], v[176:179], v[192:195], v[98:101]
	v_mfma_f32_16x16x32_bf16 v[86:89], v[168:171], v[200:203], v[86:89]
	v_mfma_f32_16x16x32_bf16 v[82:85], v[176:179], v[200:203], v[82:85]
	v_mfma_f32_16x16x32_bf16 v[70:73], v[168:171], v[208:211], v[70:73]
	v_mfma_f32_16x16x32_bf16 v[66:69], v[176:179], v[208:211], v[66:69]
	v_mfma_f32_16x16x32_bf16 v[118:121], v[172:175], v[188:191], v[118:121]
	v_mfma_f32_16x16x32_bf16 v[114:117], v[180:183], v[188:191], v[114:117]
	v_mfma_f32_16x16x32_bf16 v[102:105], v[172:175], v[196:199], v[102:105]
	v_mfma_f32_16x16x32_bf16 v[98:101], v[180:183], v[196:199], v[98:101]
	v_mfma_f32_16x16x32_bf16 v[86:89], v[172:175], v[204:207], v[86:89]
	v_mfma_f32_16x16x32_bf16 v[82:85], v[180:183], v[204:207], v[82:85]
	v_mfma_f32_16x16x32_bf16 v[70:73], v[172:175], v[212:215], v[70:73]
	v_mfma_f32_16x16x32_bf16 v[66:69], v[180:183], v[212:215], v[66:69]
	s_setprio 0
	s_barrier
	s_add_i32 s75, s41, s39
	v_lshl_add_u64 v[144:145], s[28:29], 0, v[134:135]
	s_mov_b32 m0, s75
	ds_read_b128 v[184:187], v149 offset:16384
	ds_read_b128 v[188:191], v149 offset:17408
	ds_read_b128 v[192:195], v149 offset:18432
	ds_read_b128 v[196:199], v149 offset:19456
	ds_read_b128 v[200:203], v149 offset:20480
	ds_read_b128 v[204:207], v149 offset:21504
	ds_read_b128 v[208:211], v149 offset:22528
	ds_read_b128 v[212:215], v149 offset:23552
	global_load_lds_dwordx4 v[144:145], off
	s_add_i32 m0, s75, 0x2000
	s_add_u32 s76, s28, 0x40000
	v_lshl_add_u64 v[216:217], s[28:29], 0, v[130:131]
	s_addc_u32 s77, s29, 0
	s_add_i32 s75, s48, s39
	global_load_lds_dwordx4 v[216:217], off
	v_lshl_add_u64 v[218:219], s[76:77], 0, v[134:135]
	s_mov_b32 m0, s75
	v_lshl_add_u64 v[220:221], s[30:31], 0, v[132:133]
	global_load_lds_dwordx4 v[218:219], off
	v_lshl_add_u64 v[218:219], s[76:77], 0, v[130:131]
	s_add_i32 m0, s75, 0x2000
	s_nop 0
	global_load_lds_dwordx4 v[218:219], off
	v_lshl_add_u64 v[218:219], s[30:31], 0, v[136:137]
	s_mov_b32 m0, s1
	s_nop 0
	global_load_lds_dwordx4 v[218:219], off
	s_mov_b32 m0, s43
	s_nop 0
	global_load_lds_dwordx4 v[220:221], off
	s_waitcnt vmcnt(8)
	s_waitcnt lgkmcnt(0)
	s_barrier
	s_setprio 1
	s_waitcnt lgkmcnt(0)
	v_mfma_f32_16x16x32_bf16 v[62:65], v[152:155], v[184:187], v[62:65]
	v_mfma_f32_16x16x32_bf16 v[58:61], v[160:163], v[184:187], v[58:61]
	v_mfma_f32_16x16x32_bf16 v[46:49], v[152:155], v[192:195], v[46:49]
	v_mfma_f32_16x16x32_bf16 v[42:45], v[160:163], v[192:195], v[42:45]
	v_mfma_f32_16x16x32_bf16 v[30:33], v[152:155], v[200:203], v[30:33]
	v_mfma_f32_16x16x32_bf16 v[26:29], v[160:163], v[200:203], v[26:29]
	v_mfma_f32_16x16x32_bf16 v[14:17], v[152:155], v[208:211], v[14:17]
	v_mfma_f32_16x16x32_bf16 v[10:13], v[160:163], v[208:211], v[10:13]
	v_mfma_f32_16x16x32_bf16 v[62:65], v[156:159], v[188:191], v[62:65]
	v_mfma_f32_16x16x32_bf16 v[58:61], v[164:167], v[188:191], v[58:61]
	v_mfma_f32_16x16x32_bf16 v[46:49], v[156:159], v[196:199], v[46:49]
	v_mfma_f32_16x16x32_bf16 v[42:45], v[164:167], v[196:199], v[42:45]
	v_mfma_f32_16x16x32_bf16 v[30:33], v[156:159], v[204:207], v[30:33]
	v_mfma_f32_16x16x32_bf16 v[26:29], v[164:167], v[204:207], v[26:29]
	v_mfma_f32_16x16x32_bf16 v[14:17], v[156:159], v[212:215], v[14:17]
	v_mfma_f32_16x16x32_bf16 v[10:13], v[164:167], v[212:215], v[10:13]
	s_setprio 0
	s_setprio 1
	v_mfma_f32_16x16x32_bf16 v[54:57], v[168:171], v[184:187], v[54:57]
	v_mfma_f32_16x16x32_bf16 v[50:53], v[176:179], v[184:187], v[50:53]
	v_mfma_f32_16x16x32_bf16 v[38:41], v[168:171], v[192:195], v[38:41]
	v_mfma_f32_16x16x32_bf16 v[34:37], v[176:179], v[192:195], v[34:37]
	v_mfma_f32_16x16x32_bf16 v[22:25], v[168:171], v[200:203], v[22:25]
	v_mfma_f32_16x16x32_bf16 v[18:21], v[176:179], v[200:203], v[18:21]
	v_mfma_f32_16x16x32_bf16 v[6:9], v[168:171], v[208:211], v[6:9]
	v_mfma_f32_16x16x32_bf16 v[2:5], v[176:179], v[208:211], v[2:5]
	v_mfma_f32_16x16x32_bf16 v[54:57], v[172:175], v[188:191], v[54:57]
	v_mfma_f32_16x16x32_bf16 v[50:53], v[180:183], v[188:191], v[50:53]
	v_mfma_f32_16x16x32_bf16 v[38:41], v[172:175], v[196:199], v[38:41]
	v_mfma_f32_16x16x32_bf16 v[34:37], v[180:183], v[196:199], v[34:37]
	v_mfma_f32_16x16x32_bf16 v[22:25], v[172:175], v[204:207], v[22:25]
	v_mfma_f32_16x16x32_bf16 v[18:21], v[180:183], v[204:207], v[18:21]
	v_mfma_f32_16x16x32_bf16 v[6:9], v[172:175], v[212:215], v[6:9]
	v_mfma_f32_16x16x32_bf16 v[2:5], v[180:183], v[212:215], v[2:5]
	s_setprio 0
	s_barrier
	v_add_u32_e32 v151, s49, v1
	ds_read_b128 v[152:155], v151
	ds_read_b128 v[156:159], v151 offset:1024
	ds_read_b128 v[160:163], v151 offset:2048
	ds_read_b128 v[164:167], v151 offset:3072
	v_add_u32_e32 v151, s54, v1
	ds_read_b128 v[168:171], v151
	ds_read_b128 v[172:175], v151 offset:1024
	ds_read_b128 v[176:179], v151 offset:2048
	ds_read_b128 v[180:183], v151 offset:3072
	s_add_u32 s30, s30, 0x40000
	s_addc_u32 s31, s31, 0
	s_mov_b32 m0, s44
	v_lshl_add_u64 v[222:223], s[30:31], 0, v[136:137]
	ds_read_b128 v[184:187], v149 offset:32768
	ds_read_b128 v[188:191], v149 offset:33792
	ds_read_b128 v[192:195], v149 offset:34816
	ds_read_b128 v[196:199], v149 offset:35840
	ds_read_b128 v[200:203], v149 offset:36864
	ds_read_b128 v[204:207], v149 offset:37888
	ds_read_b128 v[208:211], v149 offset:38912
	ds_read_b128 v[212:215], v149 offset:39936
	global_load_lds_dwordx4 v[222:223], off
	v_lshl_add_u64 v[222:223], s[30:31], 0, v[132:133]
	s_mov_b32 m0, s45
	s_nop 0
	global_load_lds_dwordx4 v[222:223], off
	s_waitcnt vmcnt(8)
	s_waitcnt lgkmcnt(0)
	s_barrier
	s_setprio 1
	s_waitcnt lgkmcnt(0)
	v_mfma_f32_16x16x32_bf16 v[126:129], v[152:155], v[184:187], v[126:129]
	v_mfma_f32_16x16x32_bf16 v[122:125], v[160:163], v[184:187], v[122:125]
	v_mfma_f32_16x16x32_bf16 v[110:113], v[152:155], v[192:195], v[110:113]
	v_mfma_f32_16x16x32_bf16 v[106:109], v[160:163], v[192:195], v[106:109]
	v_mfma_f32_16x16x32_bf16 v[94:97], v[152:155], v[200:203], v[94:97]
	v_mfma_f32_16x16x32_bf16 v[90:93], v[160:163], v[200:203], v[90:93]
	v_mfma_f32_16x16x32_bf16 v[78:81], v[152:155], v[208:211], v[78:81]
	v_mfma_f32_16x16x32_bf16 v[74:77], v[160:163], v[208:211], v[74:77]
	v_mfma_f32_16x16x32_bf16 v[126:129], v[156:159], v[188:191], v[126:129]
	v_mfma_f32_16x16x32_bf16 v[122:125], v[164:167], v[188:191], v[122:125]
	v_mfma_f32_16x16x32_bf16 v[110:113], v[156:159], v[196:199], v[110:113]
	v_mfma_f32_16x16x32_bf16 v[106:109], v[164:167], v[196:199], v[106:109]
	v_mfma_f32_16x16x32_bf16 v[94:97], v[156:159], v[204:207], v[94:97]
	v_mfma_f32_16x16x32_bf16 v[90:93], v[164:167], v[204:207], v[90:93]
	v_mfma_f32_16x16x32_bf16 v[78:81], v[156:159], v[212:215], v[78:81]
	v_mfma_f32_16x16x32_bf16 v[74:77], v[164:167], v[212:215], v[74:77]
	s_setprio 0
	s_setprio 1
	v_mfma_f32_16x16x32_bf16 v[118:121], v[168:171], v[184:187], v[118:121]
	v_mfma_f32_16x16x32_bf16 v[114:117], v[176:179], v[184:187], v[114:117]
	v_mfma_f32_16x16x32_bf16 v[102:105], v[168:171], v[192:195], v[102:105]
	v_mfma_f32_16x16x32_bf16 v[98:101], v[176:179], v[192:195], v[98:101]
	v_mfma_f32_16x16x32_bf16 v[86:89], v[168:171], v[200:203], v[86:89]
	v_mfma_f32_16x16x32_bf16 v[82:85], v[176:179], v[200:203], v[82:85]
	v_mfma_f32_16x16x32_bf16 v[70:73], v[168:171], v[208:211], v[70:73]
	v_mfma_f32_16x16x32_bf16 v[66:69], v[176:179], v[208:211], v[66:69]
	v_mfma_f32_16x16x32_bf16 v[118:121], v[172:175], v[188:191], v[118:121]
	v_mfma_f32_16x16x32_bf16 v[114:117], v[180:183], v[188:191], v[114:117]
	v_mfma_f32_16x16x32_bf16 v[102:105], v[172:175], v[196:199], v[102:105]
	v_mfma_f32_16x16x32_bf16 v[98:101], v[180:183], v[196:199], v[98:101]
	v_mfma_f32_16x16x32_bf16 v[86:89], v[172:175], v[204:207], v[86:89]
	v_mfma_f32_16x16x32_bf16 v[82:85], v[180:183], v[204:207], v[82:85]
	v_mfma_f32_16x16x32_bf16 v[70:73], v[172:175], v[212:215], v[70:73]
	v_mfma_f32_16x16x32_bf16 v[66:69], v[180:183], v[212:215], v[66:69]
	s_setprio 0
	s_barrier
	s_add_i32 s30, s49, s39
	v_lshl_add_u64 v[144:145], v[144:145], 0, s[4:5]
	s_mov_b32 m0, s30
	ds_read_b128 v[184:187], v149 offset:49152
	ds_read_b128 v[188:191], v149 offset:50176
	ds_read_b128 v[192:195], v149 offset:51200
	ds_read_b128 v[196:199], v149 offset:52224
	ds_read_b128 v[200:203], v149 offset:53248
	ds_read_b128 v[204:207], v149 offset:54272
	ds_read_b128 v[208:211], v149 offset:55296
	ds_read_b128 v[212:215], v149 offset:56320
	global_load_lds_dwordx4 v[144:145], off
	s_add_i32 m0, s30, 0x2000
	s_add_u32 s28, s28, 0x40080
	v_lshl_add_u64 v[144:145], v[216:217], 0, s[4:5]
	s_addc_u32 s29, s29, 0
	s_add_i32 s30, s54, s39
	global_load_lds_dwordx4 v[144:145], off
	v_lshl_add_u64 v[144:145], s[28:29], 0, v[134:135]
	s_mov_b32 m0, s30
	s_nop 0
	global_load_lds_dwordx4 v[144:145], off
	v_lshl_add_u64 v[144:145], s[28:29], 0, v[130:131]
	s_add_i32 m0, s30, 0x2000
	s_nop 0
	global_load_lds_dwordx4 v[144:145], off
	v_lshl_add_u64 v[144:145], v[218:219], 0, s[4:5]
	s_mov_b32 m0, s47
	s_nop 0
	global_load_lds_dwordx4 v[144:145], off
	v_lshl_add_u64 v[144:145], v[220:221], 0, s[4:5]
	s_mov_b32 m0, s50
	s_nop 0
	global_load_lds_dwordx4 v[144:145], off
	s_waitcnt vmcnt(8)
	s_waitcnt lgkmcnt(0)
	s_barrier
	s_setprio 1
	s_waitcnt lgkmcnt(0)
	v_mfma_f32_16x16x32_bf16 v[62:65], v[152:155], v[184:187], v[62:65]
	v_mfma_f32_16x16x32_bf16 v[58:61], v[160:163], v[184:187], v[58:61]
	v_mfma_f32_16x16x32_bf16 v[46:49], v[152:155], v[192:195], v[46:49]
	v_mfma_f32_16x16x32_bf16 v[42:45], v[160:163], v[192:195], v[42:45]
	v_mfma_f32_16x16x32_bf16 v[30:33], v[152:155], v[200:203], v[30:33]
	v_mfma_f32_16x16x32_bf16 v[26:29], v[160:163], v[200:203], v[26:29]
	v_mfma_f32_16x16x32_bf16 v[14:17], v[152:155], v[208:211], v[14:17]
	v_mfma_f32_16x16x32_bf16 v[10:13], v[160:163], v[208:211], v[10:13]
	v_mfma_f32_16x16x32_bf16 v[62:65], v[156:159], v[188:191], v[62:65]
	v_mfma_f32_16x16x32_bf16 v[58:61], v[164:167], v[188:191], v[58:61]
	v_mfma_f32_16x16x32_bf16 v[46:49], v[156:159], v[196:199], v[46:49]
	v_mfma_f32_16x16x32_bf16 v[42:45], v[164:167], v[196:199], v[42:45]
	v_mfma_f32_16x16x32_bf16 v[30:33], v[156:159], v[204:207], v[30:33]
	v_mfma_f32_16x16x32_bf16 v[26:29], v[164:167], v[204:207], v[26:29]
	v_mfma_f32_16x16x32_bf16 v[14:17], v[156:159], v[212:215], v[14:17]
	v_mfma_f32_16x16x32_bf16 v[10:13], v[164:167], v[212:215], v[10:13]
	s_setprio 0
	s_setprio 1
	v_mfma_f32_16x16x32_bf16 v[54:57], v[168:171], v[184:187], v[54:57]
	v_mfma_f32_16x16x32_bf16 v[50:53], v[176:179], v[184:187], v[50:53]
	v_mfma_f32_16x16x32_bf16 v[38:41], v[168:171], v[192:195], v[38:41]
	v_mfma_f32_16x16x32_bf16 v[34:37], v[176:179], v[192:195], v[34:37]
	v_mfma_f32_16x16x32_bf16 v[22:25], v[168:171], v[200:203], v[22:25]
	v_mfma_f32_16x16x32_bf16 v[18:21], v[176:179], v[200:203], v[18:21]
	v_mfma_f32_16x16x32_bf16 v[6:9], v[168:171], v[208:211], v[6:9]
	v_mfma_f32_16x16x32_bf16 v[2:5], v[176:179], v[208:211], v[2:5]
	v_mfma_f32_16x16x32_bf16 v[54:57], v[172:175], v[188:191], v[54:57]
	v_mfma_f32_16x16x32_bf16 v[50:53], v[180:183], v[188:191], v[50:53]
	v_mfma_f32_16x16x32_bf16 v[38:41], v[172:175], v[196:199], v[38:41]
	v_mfma_f32_16x16x32_bf16 v[34:37], v[180:183], v[196:199], v[34:37]
	v_mfma_f32_16x16x32_bf16 v[22:25], v[172:175], v[204:207], v[22:25]
	v_mfma_f32_16x16x32_bf16 v[18:21], v[180:183], v[204:207], v[18:21]
	v_mfma_f32_16x16x32_bf16 v[6:9], v[172:175], v[212:215], v[6:9]
	v_mfma_f32_16x16x32_bf16 v[2:5], v[180:183], v[212:215], v[2:5]
	s_setprio 0
	s_barrier
	s_add_i32 s74, s74, 2
	s_add_u32 s26, s26, 0x100
	s_addc_u32 s27, s27, 0
	s_add_u32 s72, s72, 0x100
	s_addc_u32 s73, s73, 0
	s_cmp_gt_u32 s74, 13
	s_cbranch_scc0 .LBB0_654
	s_and_b64 vcc, exec, s[6:7]
	s_cbranch_vccz .LBB0_657
	s_cmp_eq_u32 s46, 10
	s_cbranch_scc0 .LBB0_657
	s_barrier
.LBB0_657:
	v_mul_f32_e32 v144, 0xbfb8aa3b, v126
	v_exp_f32_e32 v144, v144
	v_mul_f32_e32 v145, 0xbfb8aa3b, v127
	v_exp_f32_e32 v145, v145
	v_mul_f32_e32 v153, 0xbfb8aa3b, v129
	v_add_f32_e32 v144, 1.0, v144
	v_rcp_f32_e32 v152, v144
	v_add_f32_e32 v144, 1.0, v145
	v_mul_f32_e32 v145, 0xbfb8aa3b, v128
	v_exp_f32_e32 v145, v145
	v_exp_f32_e32 v155, v153
	v_rcp_f32_e32 v153, v144
	s_lshl_b32 s26, s53, 7
	v_add_f32_e32 v144, 1.0, v145
	v_rcp_f32_e32 v154, v144
	v_add_f32_e32 v144, 1.0, v155
	v_rcp_f32_e32 v155, v144
	v_mul_f32_e32 v144, 0xbfb8aa3b, v122
	v_pk_mul_f32 v[126:127], v[126:127], v[152:153]
	v_mul_f32_e32 v153, 0xbfb8aa3b, v123
	v_exp_f32_e32 v156, v144
	v_exp_f32_e32 v153, v153
	v_pk_mul_f32 v[128:129], v[128:129], v[154:155]
	v_mul_f32_e32 v154, 0xbfb8aa3b, v124
	v_mul_f32_e32 v155, 0xbfb8aa3b, v125
	v_add_f32_e32 v152, 1.0, v156
	v_exp_f32_e32 v154, v154
	v_exp_f32_e32 v155, v155
	v_add_f32_e32 v153, 1.0, v153
	v_rcp_f32_e32 v152, v152
	v_rcp_f32_e32 v153, v153
	v_add_f32_e32 v154, 1.0, v154
	v_add_f32_e32 v155, 1.0, v155
	v_rcp_f32_e32 v154, v154
	v_rcp_f32_e32 v155, v155
	v_pk_mul_f32 v[118:119], v[126:127], v[118:119]
	v_pk_mul_f32 v[122:123], v[122:123], v[152:153]
	v_pk_mul_f32 v[118:119], v[118:119], s[8:9] op_sel_hi:[1,0]
	v_pk_mul_f32 v[114:115], v[122:123], v[114:115]
	v_med3_f32 v122, v118, s9, v150
	v_pk_mul_f32 v[114:115], v[114:115], s[8:9] op_sel_hi:[1,0]
	v_med3_f32 v119, v119, s9, v150
	v_mov_b32_e32 v118, 0
	v_cvt_pk_fp8_f32 v118, v122, v119
	v_med3_f32 v114, v114, s9, v150
	v_med3_f32 v115, v115, s9, v150
	v_mov_b32_e32 v119, 0
	v_pk_mul_f32 v[124:125], v[124:125], v[154:155]
	v_cvt_pk_fp8_f32 v119, v114, v115
	v_pk_mul_f32 v[120:121], v[128:129], v[120:121]
	v_pk_mul_f32 v[116:117], v[124:125], v[116:117]
	v_pk_mul_f32 v[120:121], v[120:121], s[8:9] op_sel_hi:[1,0]
	v_pk_mul_f32 v[116:117], v[116:117], s[8:9] op_sel_hi:[1,0]
	v_med3_f32 v120, v120, s9, v150
	v_med3_f32 v121, v121, s9, v150
	v_med3_f32 v114, v116, s9, v150
	v_med3_f32 v115, v117, s9, v150
	v_mul_f32_e32 v116, 0xbfb8aa3b, v110
	v_mul_f32_e32 v117, 0xbfb8aa3b, v111
	v_cvt_pk_fp8_f32 v118, v120, v121 op_sel:[0,0,1]
	v_cvt_pk_fp8_f32 v119, v114, v115 op_sel:[0,0,1]
	v_exp_f32_e32 v116, v116
	v_exp_f32_e32 v117, v117
	s_ashr_i32 s27, s26, 31
	v_lshl_add_u32 v151, s55, 8, v146
	v_lshl_add_u64 v[144:145], v[138:139], 0, s[26:27]
	v_mad_i64_i32 v[114:115], s[26:27], v151, s51, v[144:145]
	global_store_dwordx2 v[114:115], v[118:119], off
	v_add_f32_e32 v114, 1.0, v116
	v_add_f32_e32 v115, 1.0, v117
	v_mul_f32_e32 v116, 0xbfb8aa3b, v112
	v_mul_f32_e32 v117, 0xbfb8aa3b, v113
	v_exp_f32_e32 v116, v116
	v_exp_f32_e32 v117, v117
	v_rcp_f32_e32 v114, v114
	v_rcp_f32_e32 v115, v115
	v_add_f32_e32 v116, 1.0, v116
	v_add_f32_e32 v117, 1.0, v117
	v_rcp_f32_e32 v116, v116
	v_rcp_f32_e32 v117, v117
	v_mul_f32_e32 v118, 0xbfb8aa3b, v106
	v_pk_mul_f32 v[110:111], v[110:111], v[114:115]
	v_mul_f32_e32 v115, 0xbfb8aa3b, v107
	v_exp_f32_e32 v118, v118
	v_exp_f32_e32 v115, v115
	v_pk_mul_f32 v[112:113], v[112:113], v[116:117]
	v_mul_f32_e32 v116, 0xbfb8aa3b, v108
	v_mul_f32_e32 v117, 0xbfb8aa3b, v109
	v_add_f32_e32 v114, 1.0, v118
	v_exp_f32_e32 v116, v116
	v_exp_f32_e32 v117, v117
	v_add_f32_e32 v115, 1.0, v115
	v_rcp_f32_e32 v114, v114
	v_rcp_f32_e32 v115, v115
	v_add_f32_e32 v116, 1.0, v116
	v_add_f32_e32 v117, 1.0, v117
	v_rcp_f32_e32 v116, v116
	v_rcp_f32_e32 v117, v117
	v_pk_mul_f32 v[102:103], v[110:111], v[102:103]
	v_pk_mul_f32 v[106:107], v[106:107], v[114:115]
	v_pk_mul_f32 v[102:103], v[102:103], s[8:9] op_sel_hi:[1,0]
	v_pk_mul_f32 v[98:99], v[106:107], v[98:99]
	v_med3_f32 v106, v102, s9, v150
	v_pk_mul_f32 v[98:99], v[98:99], s[8:9] op_sel_hi:[1,0]
	v_med3_f32 v103, v103, s9, v150
	v_mov_b32_e32 v102, 0
	v_cvt_pk_fp8_f32 v102, v106, v103
	v_med3_f32 v98, v98, s9, v150
	v_med3_f32 v99, v99, s9, v150
	v_mov_b32_e32 v103, 0
	v_pk_mul_f32 v[108:109], v[108:109], v[116:117]
	v_cvt_pk_fp8_f32 v103, v98, v99
	v_pk_mul_f32 v[104:105], v[112:113], v[104:105]
	v_pk_mul_f32 v[100:101], v[108:109], v[100:101]
	v_pk_mul_f32 v[104:105], v[104:105], s[8:9] op_sel_hi:[1,0]
	v_pk_mul_f32 v[100:101], v[100:101], s[8:9] op_sel_hi:[1,0]
	v_med3_f32 v104, v104, s9, v150
	v_med3_f32 v105, v105, s9, v150
	v_med3_f32 v98, v100, s9, v150
	v_med3_f32 v99, v101, s9, v150
	v_mul_f32_e32 v100, 0xbfb8aa3b, v94
	v_mul_f32_e32 v101, 0xbfb8aa3b, v95
	v_cvt_pk_fp8_f32 v102, v104, v105 op_sel:[0,0,1]
	v_cvt_pk_fp8_f32 v103, v98, v99 op_sel:[0,0,1]
	v_exp_f32_e32 v100, v100
	v_exp_f32_e32 v101, v101
	v_or_b32_e32 v119, 16, v151
	v_mad_i64_i32 v[98:99], s[26:27], v119, s51, v[144:145]
	global_store_dwordx2 v[98:99], v[102:103], off
	v_add_f32_e32 v98, 1.0, v100
	v_add_f32_e32 v99, 1.0, v101
	v_mul_f32_e32 v100, 0xbfb8aa3b, v96
	v_mul_f32_e32 v101, 0xbfb8aa3b, v97
	v_exp_f32_e32 v100, v100
	v_exp_f32_e32 v101, v101
	v_rcp_f32_e32 v98, v98
	v_rcp_f32_e32 v99, v99
	v_add_f32_e32 v100, 1.0, v100
	v_add_f32_e32 v101, 1.0, v101
	v_rcp_f32_e32 v100, v100
	v_rcp_f32_e32 v101, v101
	v_mul_f32_e32 v102, 0xbfb8aa3b, v90
	v_pk_mul_f32 v[94:95], v[94:95], v[98:99]
	v_mul_f32_e32 v99, 0xbfb8aa3b, v91
	v_exp_f32_e32 v102, v102
	v_exp_f32_e32 v99, v99
	v_pk_mul_f32 v[96:97], v[96:97], v[100:101]
	v_mul_f32_e32 v100, 0xbfb8aa3b, v92
	v_mul_f32_e32 v101, 0xbfb8aa3b, v93
	v_add_f32_e32 v98, 1.0, v102
	v_exp_f32_e32 v100, v100
	v_exp_f32_e32 v101, v101
	v_add_f32_e32 v99, 1.0, v99
	v_rcp_f32_e32 v98, v98
	v_rcp_f32_e32 v99, v99
	v_add_f32_e32 v100, 1.0, v100
	v_add_f32_e32 v101, 1.0, v101
	v_rcp_f32_e32 v100, v100
	v_rcp_f32_e32 v101, v101
	v_pk_mul_f32 v[86:87], v[94:95], v[86:87]
	v_pk_mul_f32 v[90:91], v[90:91], v[98:99]
	v_pk_mul_f32 v[86:87], v[86:87], s[8:9] op_sel_hi:[1,0]
	v_pk_mul_f32 v[82:83], v[90:91], v[82:83]
	v_med3_f32 v90, v86, s9, v150
	v_pk_mul_f32 v[82:83], v[82:83], s[8:9] op_sel_hi:[1,0]
	v_med3_f32 v87, v87, s9, v150
	v_mov_b32_e32 v86, 0
	v_cvt_pk_fp8_f32 v86, v90, v87
	v_med3_f32 v82, v82, s9, v150
	v_med3_f32 v83, v83, s9, v150
	v_mov_b32_e32 v87, 0
	v_pk_mul_f32 v[92:93], v[92:93], v[100:101]
	v_cvt_pk_fp8_f32 v87, v82, v83
	v_pk_mul_f32 v[88:89], v[96:97], v[88:89]
	v_pk_mul_f32 v[84:85], v[92:93], v[84:85]
	v_pk_mul_f32 v[88:89], v[88:89], s[8:9] op_sel_hi:[1,0]
	v_pk_mul_f32 v[84:85], v[84:85], s[8:9] op_sel_hi:[1,0]
	v_med3_f32 v88, v88, s9, v150
	v_med3_f32 v89, v89, s9, v150
	v_med3_f32 v82, v84, s9, v150
	v_med3_f32 v83, v85, s9, v150
	v_mul_f32_e32 v84, 0xbfb8aa3b, v78
	v_mul_f32_e32 v85, 0xbfb8aa3b, v79
	v_cvt_pk_fp8_f32 v86, v88, v89 op_sel:[0,0,1]
	v_cvt_pk_fp8_f32 v87, v82, v83 op_sel:[0,0,1]
	v_exp_f32_e32 v84, v84
	v_exp_f32_e32 v85, v85
	v_or_b32_e32 v103, 32, v151
	v_mad_i64_i32 v[82:83], s[26:27], v103, s51, v[144:145]
	global_store_dwordx2 v[82:83], v[86:87], off
	v_add_f32_e32 v82, 1.0, v84
	v_add_f32_e32 v83, 1.0, v85
	v_mul_f32_e32 v84, 0xbfb8aa3b, v80
	v_mul_f32_e32 v85, 0xbfb8aa3b, v81
	v_exp_f32_e32 v84, v84
	v_exp_f32_e32 v85, v85
	v_rcp_f32_e32 v82, v82
	v_rcp_f32_e32 v83, v83
	v_add_f32_e32 v84, 1.0, v84
	v_add_f32_e32 v85, 1.0, v85
	v_rcp_f32_e32 v84, v84
	v_rcp_f32_e32 v85, v85
	v_mul_f32_e32 v86, 0xbfb8aa3b, v74
	v_pk_mul_f32 v[78:79], v[78:79], v[82:83]
	v_mul_f32_e32 v83, 0xbfb8aa3b, v75
	v_exp_f32_e32 v86, v86
	v_exp_f32_e32 v83, v83
	v_pk_mul_f32 v[80:81], v[80:81], v[84:85]
	v_mul_f32_e32 v84, 0xbfb8aa3b, v76
	v_mul_f32_e32 v85, 0xbfb8aa3b, v77
	v_add_f32_e32 v82, 1.0, v86
	v_exp_f32_e32 v84, v84
	v_exp_f32_e32 v85, v85
	v_add_f32_e32 v83, 1.0, v83
	v_rcp_f32_e32 v82, v82
	v_rcp_f32_e32 v83, v83
	v_add_f32_e32 v84, 1.0, v84
	v_add_f32_e32 v85, 1.0, v85
	v_rcp_f32_e32 v84, v84
	v_rcp_f32_e32 v85, v85
	v_pk_mul_f32 v[70:71], v[78:79], v[70:71]
	v_pk_mul_f32 v[74:75], v[74:75], v[82:83]
	v_pk_mul_f32 v[70:71], v[70:71], s[8:9] op_sel_hi:[1,0]
	v_pk_mul_f32 v[66:67], v[74:75], v[66:67]
	v_med3_f32 v74, v70, s9, v150
	v_pk_mul_f32 v[66:67], v[66:67], s[8:9] op_sel_hi:[1,0]
	v_med3_f32 v71, v71, s9, v150
	v_mov_b32_e32 v70, 0
	v_cvt_pk_fp8_f32 v70, v74, v71
	v_med3_f32 v66, v66, s9, v150
	v_med3_f32 v67, v67, s9, v150
	v_mov_b32_e32 v71, 0
	v_pk_mul_f32 v[76:77], v[76:77], v[84:85]
	v_cvt_pk_fp8_f32 v71, v66, v67
	v_pk_mul_f32 v[72:73], v[80:81], v[72:73]
	v_pk_mul_f32 v[68:69], v[76:77], v[68:69]
	v_pk_mul_f32 v[72:73], v[72:73], s[8:9] op_sel_hi:[1,0]
	v_pk_mul_f32 v[68:69], v[68:69], s[8:9] op_sel_hi:[1,0]
	v_med3_f32 v72, v72, s9, v150
	v_med3_f32 v73, v73, s9, v150
	v_med3_f32 v66, v68, s9, v150
	v_med3_f32 v67, v69, s9, v150
	v_mul_f32_e32 v68, 0xbfb8aa3b, v62
	v_mul_f32_e32 v69, 0xbfb8aa3b, v63
	v_cvt_pk_fp8_f32 v70, v72, v73 op_sel:[0,0,1]
	v_cvt_pk_fp8_f32 v71, v66, v67 op_sel:[0,0,1]
	v_exp_f32_e32 v68, v68
	v_exp_f32_e32 v69, v69
	v_or_b32_e32 v87, 48, v151
	v_mad_i64_i32 v[66:67], s[26:27], v87, s51, v[144:145]
	global_store_dwordx2 v[66:67], v[70:71], off
	v_add_f32_e32 v66, 1.0, v68
	v_add_f32_e32 v67, 1.0, v69
	v_mul_f32_e32 v68, 0xbfb8aa3b, v64
	v_mul_f32_e32 v69, 0xbfb8aa3b, v65
	v_exp_f32_e32 v68, v68
	v_exp_f32_e32 v69, v69
	v_rcp_f32_e32 v66, v66
	v_rcp_f32_e32 v67, v67
	v_add_f32_e32 v68, 1.0, v68
	v_add_f32_e32 v69, 1.0, v69
	v_rcp_f32_e32 v68, v68
	v_rcp_f32_e32 v69, v69
	v_mul_f32_e32 v70, 0xbfb8aa3b, v58
	v_pk_mul_f32 v[62:63], v[62:63], v[66:67]
	v_mul_f32_e32 v67, 0xbfb8aa3b, v59
	v_exp_f32_e32 v70, v70
	v_exp_f32_e32 v67, v67
	v_pk_mul_f32 v[64:65], v[64:65], v[68:69]
	v_mul_f32_e32 v68, 0xbfb8aa3b, v60
	v_mul_f32_e32 v69, 0xbfb8aa3b, v61
	v_add_f32_e32 v66, 1.0, v70
	v_exp_f32_e32 v68, v68
	v_exp_f32_e32 v69, v69
	v_add_f32_e32 v67, 1.0, v67
	v_rcp_f32_e32 v66, v66
	v_rcp_f32_e32 v67, v67
	v_add_f32_e32 v68, 1.0, v68
	v_add_f32_e32 v69, 1.0, v69
	v_rcp_f32_e32 v68, v68
	v_rcp_f32_e32 v69, v69
	v_pk_mul_f32 v[54:55], v[62:63], v[54:55]
	v_pk_mul_f32 v[58:59], v[58:59], v[66:67]
	v_pk_mul_f32 v[54:55], v[54:55], s[8:9] op_sel_hi:[1,0]
	v_pk_mul_f32 v[50:51], v[58:59], v[50:51]
	v_med3_f32 v58, v54, s9, v150
	v_pk_mul_f32 v[50:51], v[50:51], s[8:9] op_sel_hi:[1,0]
	v_med3_f32 v55, v55, s9, v150
	v_mov_b32_e32 v54, 0
	v_cvt_pk_fp8_f32 v54, v58, v55
	v_med3_f32 v50, v50, s9, v150
	v_med3_f32 v51, v51, s9, v150
	v_mov_b32_e32 v55, 0
	v_pk_mul_f32 v[60:61], v[60:61], v[68:69]
	v_cvt_pk_fp8_f32 v55, v50, v51
	v_pk_mul_f32 v[56:57], v[64:65], v[56:57]
	v_pk_mul_f32 v[52:53], v[60:61], v[52:53]
	v_pk_mul_f32 v[56:57], v[56:57], s[8:9] op_sel_hi:[1,0]
	v_pk_mul_f32 v[52:53], v[52:53], s[8:9] op_sel_hi:[1,0]
	v_med3_f32 v56, v56, s9, v150
	v_med3_f32 v57, v57, s9, v150
	v_med3_f32 v50, v52, s9, v150
	v_med3_f32 v51, v53, s9, v150
	v_mul_f32_e32 v52, 0xbfb8aa3b, v46
	v_mul_f32_e32 v53, 0xbfb8aa3b, v47
	v_cvt_pk_fp8_f32 v54, v56, v57 op_sel:[0,0,1]
	v_cvt_pk_fp8_f32 v55, v50, v51 op_sel:[0,0,1]
	v_exp_f32_e32 v52, v52
	v_exp_f32_e32 v53, v53
	v_add_u32_e32 v71, 0x80, v151
	v_mad_i64_i32 v[50:51], s[26:27], v71, s51, v[144:145]
	global_store_dwordx2 v[50:51], v[54:55], off
	v_add_f32_e32 v50, 1.0, v52
	v_add_f32_e32 v51, 1.0, v53
	v_mul_f32_e32 v52, 0xbfb8aa3b, v48
	v_mul_f32_e32 v53, 0xbfb8aa3b, v49
	v_exp_f32_e32 v52, v52
	v_exp_f32_e32 v53, v53
	v_rcp_f32_e32 v50, v50
	v_rcp_f32_e32 v51, v51
	v_add_f32_e32 v52, 1.0, v52
	v_add_f32_e32 v53, 1.0, v53
	v_rcp_f32_e32 v52, v52
	v_rcp_f32_e32 v53, v53
	v_mul_f32_e32 v54, 0xbfb8aa3b, v42
	v_pk_mul_f32 v[46:47], v[46:47], v[50:51]
	v_mul_f32_e32 v51, 0xbfb8aa3b, v43
	v_exp_f32_e32 v54, v54
	v_exp_f32_e32 v51, v51
	v_pk_mul_f32 v[48:49], v[48:49], v[52:53]
	v_mul_f32_e32 v52, 0xbfb8aa3b, v44
	v_mul_f32_e32 v53, 0xbfb8aa3b, v45
	v_add_f32_e32 v50, 1.0, v54
	v_exp_f32_e32 v52, v52
	v_exp_f32_e32 v53, v53
	v_add_f32_e32 v51, 1.0, v51
	v_rcp_f32_e32 v50, v50
	v_rcp_f32_e32 v51, v51
	v_add_f32_e32 v52, 1.0, v52
	v_add_f32_e32 v53, 1.0, v53
	v_rcp_f32_e32 v52, v52
	v_rcp_f32_e32 v53, v53
	v_pk_mul_f32 v[38:39], v[46:47], v[38:39]
	v_pk_mul_f32 v[42:43], v[42:43], v[50:51]
	v_pk_mul_f32 v[38:39], v[38:39], s[8:9] op_sel_hi:[1,0]
	v_pk_mul_f32 v[34:35], v[42:43], v[34:35]
	v_med3_f32 v42, v38, s9, v150
	v_pk_mul_f32 v[34:35], v[34:35], s[8:9] op_sel_hi:[1,0]
	v_med3_f32 v39, v39, s9, v150
	v_mov_b32_e32 v38, 0
	v_cvt_pk_fp8_f32 v38, v42, v39
	v_med3_f32 v34, v34, s9, v150
	v_med3_f32 v35, v35, s9, v150
	v_mov_b32_e32 v39, 0
	v_pk_mul_f32 v[44:45], v[44:45], v[52:53]
	v_cvt_pk_fp8_f32 v39, v34, v35
	v_pk_mul_f32 v[40:41], v[48:49], v[40:41]
	v_pk_mul_f32 v[36:37], v[44:45], v[36:37]
	v_pk_mul_f32 v[40:41], v[40:41], s[8:9] op_sel_hi:[1,0]
	v_pk_mul_f32 v[36:37], v[36:37], s[8:9] op_sel_hi:[1,0]
	v_med3_f32 v40, v40, s9, v150
	v_med3_f32 v41, v41, s9, v150
	v_med3_f32 v34, v36, s9, v150
	v_med3_f32 v35, v37, s9, v150
	v_mul_f32_e32 v36, 0xbfb8aa3b, v30
	v_mul_f32_e32 v37, 0xbfb8aa3b, v31
	v_cvt_pk_fp8_f32 v38, v40, v41 op_sel:[0,0,1]
	v_cvt_pk_fp8_f32 v39, v34, v35 op_sel:[0,0,1]
	v_exp_f32_e32 v36, v36
	v_exp_f32_e32 v37, v37
	v_add_u32_e32 v55, 0x90, v151
	v_mad_i64_i32 v[34:35], s[26:27], v55, s51, v[144:145]
	global_store_dwordx2 v[34:35], v[38:39], off
	v_add_f32_e32 v34, 1.0, v36
	v_add_f32_e32 v35, 1.0, v37
	v_mul_f32_e32 v36, 0xbfb8aa3b, v32
	v_mul_f32_e32 v37, 0xbfb8aa3b, v33
	v_exp_f32_e32 v36, v36
	v_exp_f32_e32 v37, v37
	v_rcp_f32_e32 v34, v34
	v_rcp_f32_e32 v35, v35
	v_add_f32_e32 v36, 1.0, v36
	v_add_f32_e32 v37, 1.0, v37
	v_rcp_f32_e32 v36, v36
	v_rcp_f32_e32 v37, v37
	v_mul_f32_e32 v38, 0xbfb8aa3b, v26
	v_pk_mul_f32 v[30:31], v[30:31], v[34:35]
	v_mul_f32_e32 v35, 0xbfb8aa3b, v27
	v_exp_f32_e32 v38, v38
	v_exp_f32_e32 v35, v35
	v_pk_mul_f32 v[32:33], v[32:33], v[36:37]
	v_mul_f32_e32 v36, 0xbfb8aa3b, v28
	v_mul_f32_e32 v37, 0xbfb8aa3b, v29
	v_add_f32_e32 v34, 1.0, v38
	v_exp_f32_e32 v36, v36
	v_exp_f32_e32 v37, v37
	v_add_f32_e32 v35, 1.0, v35
	v_rcp_f32_e32 v34, v34
	v_rcp_f32_e32 v35, v35
	v_add_f32_e32 v36, 1.0, v36
	v_add_f32_e32 v37, 1.0, v37
	v_rcp_f32_e32 v36, v36
	v_rcp_f32_e32 v37, v37
	v_pk_mul_f32 v[22:23], v[30:31], v[22:23]
	v_pk_mul_f32 v[26:27], v[26:27], v[34:35]
	v_pk_mul_f32 v[22:23], v[22:23], s[8:9] op_sel_hi:[1,0]
	v_pk_mul_f32 v[18:19], v[26:27], v[18:19]
	v_med3_f32 v26, v22, s9, v150
	v_pk_mul_f32 v[18:19], v[18:19], s[8:9] op_sel_hi:[1,0]
	v_med3_f32 v23, v23, s9, v150
	v_mov_b32_e32 v22, 0
	v_cvt_pk_fp8_f32 v22, v26, v23
	v_med3_f32 v18, v18, s9, v150
	v_med3_f32 v19, v19, s9, v150
	v_mov_b32_e32 v23, 0
	v_pk_mul_f32 v[28:29], v[28:29], v[36:37]
	v_cvt_pk_fp8_f32 v23, v18, v19
	v_pk_mul_f32 v[20:21], v[28:29], v[20:21]
	v_pk_mul_f32 v[24:25], v[32:33], v[24:25]
	v_pk_mul_f32 v[20:21], v[20:21], s[8:9] op_sel_hi:[1,0]
	v_pk_mul_f32 v[24:25], v[24:25], s[8:9] op_sel_hi:[1,0]
	v_med3_f32 v18, v20, s9, v150
	v_med3_f32 v19, v21, s9, v150
	v_cvt_pk_fp8_f32 v23, v18, v19 op_sel:[0,0,1]
	v_mul_f32_e32 v18, 0xbfb8aa3b, v14
	v_exp_f32_e32 v20, v18
	v_mul_f32_e32 v18, 0xbfb8aa3b, v15
	v_med3_f32 v24, v24, s9, v150
	v_med3_f32 v25, v25, s9, v150
	v_exp_f32_e32 v21, v18
	v_cvt_pk_fp8_f32 v22, v24, v25 op_sel:[0,0,1]
	v_add_u32_e32 v39, 0xa0, v151
	v_mad_i64_i32 v[18:19], s[26:27], v39, s51, v[144:145]
	v_add_f32_e32 v20, 1.0, v20
	v_add_f32_e32 v21, 1.0, v21
	v_rcp_f32_e32 v20, v20
	v_rcp_f32_e32 v21, v21
	v_mul_f32_e32 v26, 0xbfb8aa3b, v10
	global_store_dwordx2 v[18:19], v[22:23], off
	v_mul_f32_e32 v19, 0xbfb8aa3b, v11
	v_exp_f32_e32 v26, v26
	v_exp_f32_e32 v19, v19
	v_mul_f32_e32 v24, 0xbfb8aa3b, v16
	v_mul_f32_e32 v25, 0xbfb8aa3b, v17
	v_pk_mul_f32 v[14:15], v[14:15], v[20:21]
	v_mul_f32_e32 v20, 0xbfb8aa3b, v12
	v_mul_f32_e32 v21, 0xbfb8aa3b, v13
	v_exp_f32_e32 v24, v24
	v_exp_f32_e32 v25, v25
	v_add_f32_e32 v18, 1.0, v26
	v_exp_f32_e32 v20, v20
	v_exp_f32_e32 v21, v21
	v_add_f32_e32 v19, 1.0, v19
	v_rcp_f32_e32 v18, v18
	v_rcp_f32_e32 v19, v19
	v_add_f32_e32 v24, 1.0, v24
	v_add_f32_e32 v25, 1.0, v25
	v_add_f32_e32 v20, 1.0, v20
	v_add_f32_e32 v21, 1.0, v21
	v_rcp_f32_e32 v24, v24
	v_rcp_f32_e32 v25, v25
	v_rcp_f32_e32 v20, v20
	v_rcp_f32_e32 v21, v21
	v_pk_mul_f32 v[6:7], v[14:15], v[6:7]
	v_pk_mul_f32 v[10:11], v[10:11], v[18:19]
	v_pk_mul_f32 v[6:7], v[6:7], s[8:9] op_sel_hi:[1,0]
	v_pk_mul_f32 v[2:3], v[10:11], v[2:3]
	v_med3_f32 v10, v6, s9, v150
	v_pk_mul_f32 v[2:3], v[2:3], s[8:9] op_sel_hi:[1,0]
	v_med3_f32 v7, v7, s9, v150
	v_mov_b32_e32 v6, 0
	v_cvt_pk_fp8_f32 v6, v10, v7
	v_med3_f32 v2, v2, s9, v150
	v_med3_f32 v3, v3, s9, v150
	v_mov_b32_e32 v7, 0
	v_pk_mul_f32 v[16:17], v[16:17], v[24:25]
	v_pk_mul_f32 v[12:13], v[12:13], v[20:21]
	v_cvt_pk_fp8_f32 v7, v2, v3
	v_pk_mul_f32 v[8:9], v[16:17], v[8:9]
	v_pk_mul_f32 v[4:5], v[12:13], v[4:5]
	v_pk_mul_f32 v[8:9], v[8:9], s[8:9] op_sel_hi:[1,0]
	v_pk_mul_f32 v[4:5], v[4:5], s[8:9] op_sel_hi:[1,0]
	v_med3_f32 v8, v8, s9, v150
	v_med3_f32 v9, v9, s9, v150
	v_med3_f32 v2, v4, s9, v150
	v_med3_f32 v3, v5, s9, v150
	v_cvt_pk_fp8_f32 v6, v8, v9 op_sel:[0,0,1]
	v_cvt_pk_fp8_f32 v7, v2, v3 op_sel:[0,0,1]
	v_add_u32_e32 v2, 0xb0, v151
	v_mad_i64_i32 v[2:3], s[26:27], v2, s51, v[144:145]
	s_cmp_eq_u32 s46, 10
	s_mov_b64 s[26:27], -1
	global_store_dwordx2 v[2:3], v[6:7], off
	s_cbranch_scc1 .LBB0_650
	s_andn2_b64 vcc, exec, s[2:3]
	s_cbranch_vccnz .LBB0_649
	s_branch .LBB0_649

.LBB0_1391:
	s_and_b64 vcc, exec, s[82:83]
	s_cbranch_vccz .LBB0_1393
	s_and_b64 vcc, exec, s[92:93]
	s_cbranch_vccnz .LBB0_1393
	s_barrier
.LBB0_1393:
	v_mul_f32_e32 v5, 0xbfb8aa3b, v190
	v_exp_f32_e32 v5, v5
	s_lshl_b32 s38, s42, 8
	v_mov_b32_e32 v2, v0
	s_add_i32 s38, s38, s31
	v_add_f32_e32 v5, 1.0, v5
	v_rcp_f32_e32 v6, v5
	v_mul_f32_e32 v5, 0xbfb8aa3b, v191
	v_exp_f32_e32 v5, v5
	s_nop 0
	v_and_or_b32 v4, v2, 15, s38
	v_add_f32_e32 v5, 1.0, v5
	v_rcp_f32_e32 v7, v5
	v_mul_f32_e32 v5, 0xbfb8aa3b, v192
	v_exp_f32_e32 v5, v5
	s_lshl_b32 s38, s45, 7
	v_pk_mul_f32 v[6:7], v[190:191], v[6:7]
	s_ashr_i32 s39, s38, 31
	v_add_f32_e32 v5, 1.0, v5
	v_rcp_f32_e32 v8, v5
	v_mul_f32_e32 v5, 0xbfb8aa3b, v193
	v_exp_f32_e32 v5, v5
	v_pk_mul_f32 v[6:7], v[6:7], v[186:187]
	v_lshrrev_b32_e32 v2, 1, v2
	v_pk_mul_f32 v[6:7], v[6:7], s[66:67] op_sel_hi:[1,0]
	v_add_f32_e32 v5, 1.0, v5
	v_rcp_f32_e32 v9, v5
	v_mul_f32_e32 v5, 0xbfb8aa3b, v182
	v_exp_f32_e32 v5, v5
	v_med3_f32 v7, v7, s29, v1
	v_pk_mul_f32 v[8:9], v[192:193], v[8:9]
	s_add_u32 s38, s5, s38
	v_add_f32_e32 v5, 1.0, v5
	v_rcp_f32_e32 v10, v5
	v_mul_f32_e32 v5, 0xbfb8aa3b, v183
	v_exp_f32_e32 v5, v5
	v_pk_mul_f32 v[8:9], v[8:9], v[188:189]
	v_and_or_b32 v194, v2, 24, s25
	v_pk_mul_f32 v[8:9], v[8:9], s[66:67] op_sel_hi:[1,0]
	v_add_f32_e32 v5, 1.0, v5
	v_rcp_f32_e32 v11, v5
	v_mul_f32_e32 v5, 0xbfb8aa3b, v184
	v_exp_f32_e32 v5, v5
	s_addc_u32 s39, s4, s39
	v_pk_mul_f32 v[10:11], v[182:183], v[10:11]
	v_lshl_add_u64 v[2:3], s[38:39], 0, v[194:195]
	v_add_f32_e32 v5, 1.0, v5
	v_rcp_f32_e32 v12, v5
	v_mul_f32_e32 v5, 0xbfb8aa3b, v185
	v_exp_f32_e32 v5, v5
	v_pk_mul_f32 v[10:11], v[10:11], v[178:179]
	s_andn2_b64 vcc, exec, s[92:93]
	v_pk_mul_f32 v[10:11], v[10:11], s[66:67] op_sel_hi:[1,0]
	v_add_f32_e32 v5, 1.0, v5
	v_rcp_f32_e32 v13, v5
	v_med3_f32 v5, v6, s29, v1
	v_mov_b32_e32 v6, v195
	v_cvt_pk_fp8_f32 v6, v5, v7
	v_med3_f32 v5, v8, s29, v1
	v_med3_f32 v7, v9, s29, v1
	v_med3_f32 v8, v11, s29, v1
	v_cvt_pk_fp8_f32 v6, v5, v7 op_sel:[0,0,1]
	v_med3_f32 v5, v10, s29, v1
	v_mov_b32_e32 v7, v195
	v_pk_mul_f32 v[12:13], v[184:185], v[12:13]
	v_cvt_pk_fp8_f32 v7, v5, v8
	v_pk_mul_f32 v[12:13], v[12:13], v[180:181]
	v_mul_f32_e32 v10, 0xbfb8aa3b, v166
	v_pk_mul_f32 v[12:13], v[12:13], s[66:67] op_sel_hi:[1,0]
	v_mul_f32_e32 v11, 0xbfb8aa3b, v167
	v_med3_f32 v5, v12, s29, v1
	v_med3_f32 v8, v13, s29, v1
	v_cvt_pk_fp8_f32 v7, v5, v8 op_sel:[0,0,1]
	v_mad_i64_i32 v[8:9], s[38:39], v4, s2, v[2:3]
	v_exp_f32_e32 v10, v10
	global_store_dwordx2 v[8:9], v[6:7], off
	v_mul_f32_e32 v6, 0xbfb8aa3b, v174
	v_mul_f32_e32 v7, 0xbfb8aa3b, v175
	v_exp_f32_e32 v6, v6
	v_exp_f32_e32 v7, v7
	v_mul_f32_e32 v8, 0xbfb8aa3b, v176
	v_mul_f32_e32 v9, 0xbfb8aa3b, v177
	v_add_f32_e32 v6, 1.0, v6
	v_add_f32_e32 v7, 1.0, v7
	v_exp_f32_e32 v8, v8
	v_exp_f32_e32 v9, v9
	v_rcp_f32_e32 v6, v6
	v_rcp_f32_e32 v7, v7
	v_exp_f32_e32 v11, v11
	v_add_f32_e32 v8, 1.0, v8
	v_add_f32_e32 v9, 1.0, v9
	v_mul_f32_e32 v12, 0xbfb8aa3b, v168
	v_mul_f32_e32 v13, 0xbfb8aa3b, v169
	v_rcp_f32_e32 v8, v8
	v_rcp_f32_e32 v9, v9
	v_pk_mul_f32 v[6:7], v[174:175], v[6:7]
	v_add_f32_e32 v10, 1.0, v10
	v_add_f32_e32 v11, 1.0, v11
	v_exp_f32_e32 v12, v12
	v_exp_f32_e32 v13, v13
	v_pk_mul_f32 v[6:7], v[6:7], v[170:171]
	v_rcp_f32_e32 v10, v10
	v_rcp_f32_e32 v11, v11
	v_pk_mul_f32 v[6:7], v[6:7], s[66:67] op_sel_hi:[1,0]
	v_pk_mul_f32 v[8:9], v[176:177], v[8:9]
	v_med3_f32 v14, v6, s29, v1
	v_med3_f32 v7, v7, s29, v1
	v_mov_b32_e32 v6, v195
	v_add_f32_e32 v12, 1.0, v12
	v_add_f32_e32 v13, 1.0, v13
	v_cvt_pk_fp8_f32 v6, v14, v7
	v_pk_mul_f32 v[8:9], v[8:9], v[172:173]
	v_rcp_f32_e32 v12, v12
	v_rcp_f32_e32 v13, v13
	v_pk_mul_f32 v[10:11], v[166:167], v[10:11]
	v_pk_mul_f32 v[8:9], v[8:9], s[66:67] op_sel_hi:[1,0]
	v_pk_mul_f32 v[10:11], v[10:11], v[162:163]
	v_med3_f32 v7, v8, s29, v1
	v_pk_mul_f32 v[10:11], v[10:11], s[66:67] op_sel_hi:[1,0]
	v_med3_f32 v8, v9, s29, v1
	v_cvt_pk_fp8_f32 v6, v7, v8 op_sel:[0,0,1]
	v_med3_f32 v8, v10, s29, v1
	v_med3_f32 v9, v11, s29, v1
	v_mov_b32_e32 v7, v195
	v_pk_mul_f32 v[12:13], v[168:169], v[12:13]
	v_cvt_pk_fp8_f32 v7, v8, v9
	v_pk_mul_f32 v[12:13], v[12:13], v[164:165]
	v_or_b32_e32 v5, 16, v4
	v_pk_mul_f32 v[12:13], v[12:13], s[66:67] op_sel_hi:[1,0]
	v_mul_f32_e32 v10, 0xbfb8aa3b, v150
	v_med3_f32 v8, v12, s29, v1
	v_med3_f32 v9, v13, s29, v1
	v_cvt_pk_fp8_f32 v7, v8, v9 op_sel:[0,0,1]
	v_mad_i64_i32 v[8:9], s[38:39], v5, s2, v[2:3]
	v_mul_f32_e32 v11, 0xbfb8aa3b, v151
	global_store_dwordx2 v[8:9], v[6:7], off
	v_mul_f32_e32 v6, 0xbfb8aa3b, v158
	v_mul_f32_e32 v7, 0xbfb8aa3b, v159
	v_exp_f32_e32 v6, v6
	v_exp_f32_e32 v7, v7
	v_mul_f32_e32 v8, 0xbfb8aa3b, v160
	v_mul_f32_e32 v9, 0xbfb8aa3b, v161
	v_add_f32_e32 v6, 1.0, v6
	v_add_f32_e32 v7, 1.0, v7
	v_exp_f32_e32 v8, v8
	v_exp_f32_e32 v9, v9
	v_rcp_f32_e32 v6, v6
	v_rcp_f32_e32 v7, v7
	v_exp_f32_e32 v10, v10
	v_exp_f32_e32 v11, v11
	v_add_f32_e32 v8, 1.0, v8
	v_add_f32_e32 v9, 1.0, v9
	v_mul_f32_e32 v12, 0xbfb8aa3b, v152
	v_mul_f32_e32 v13, 0xbfb8aa3b, v153
	v_rcp_f32_e32 v8, v8
	v_rcp_f32_e32 v9, v9
	v_pk_mul_f32 v[6:7], v[158:159], v[6:7]
	v_add_f32_e32 v10, 1.0, v10
	v_add_f32_e32 v11, 1.0, v11
	v_exp_f32_e32 v12, v12
	v_exp_f32_e32 v13, v13
	v_pk_mul_f32 v[6:7], v[6:7], v[154:155]
	v_rcp_f32_e32 v10, v10
	v_rcp_f32_e32 v11, v11
	v_pk_mul_f32 v[6:7], v[6:7], s[66:67] op_sel_hi:[1,0]
	v_pk_mul_f32 v[8:9], v[160:161], v[8:9]
	v_med3_f32 v14, v6, s29, v1
	v_med3_f32 v7, v7, s29, v1
	v_mov_b32_e32 v6, v195
	v_add_f32_e32 v12, 1.0, v12
	v_add_f32_e32 v13, 1.0, v13
	v_cvt_pk_fp8_f32 v6, v14, v7
	v_pk_mul_f32 v[8:9], v[8:9], v[156:157]
	v_rcp_f32_e32 v12, v12
	v_rcp_f32_e32 v13, v13
	v_pk_mul_f32 v[10:11], v[150:151], v[10:11]
	v_pk_mul_f32 v[8:9], v[8:9], s[66:67] op_sel_hi:[1,0]
	v_pk_mul_f32 v[10:11], v[10:11], v[146:147]
	v_med3_f32 v7, v8, s29, v1
	v_pk_mul_f32 v[10:11], v[10:11], s[66:67] op_sel_hi:[1,0]
	v_med3_f32 v8, v9, s29, v1
	v_cvt_pk_fp8_f32 v6, v7, v8 op_sel:[0,0,1]
	v_med3_f32 v8, v10, s29, v1
	v_med3_f32 v9, v11, s29, v1
	v_mov_b32_e32 v7, v195
	v_pk_mul_f32 v[12:13], v[152:153], v[12:13]
	v_cvt_pk_fp8_f32 v7, v8, v9
	v_pk_mul_f32 v[12:13], v[12:13], v[148:149]
	v_or_b32_e32 v5, 32, v4
	v_pk_mul_f32 v[12:13], v[12:13], s[66:67] op_sel_hi:[1,0]
	v_mul_f32_e32 v10, 0xbfb8aa3b, v134
	v_med3_f32 v8, v12, s29, v1
	v_med3_f32 v9, v13, s29, v1
	v_cvt_pk_fp8_f32 v7, v8, v9 op_sel:[0,0,1]
	v_mad_i64_i32 v[8:9], s[38:39], v5, s2, v[2:3]
	v_mul_f32_e32 v11, 0xbfb8aa3b, v135
	global_store_dwordx2 v[8:9], v[6:7], off
	v_mul_f32_e32 v6, 0xbfb8aa3b, v142
	v_mul_f32_e32 v7, 0xbfb8aa3b, v143
	v_exp_f32_e32 v6, v6
	v_exp_f32_e32 v7, v7
	v_mul_f32_e32 v8, 0xbfb8aa3b, v144
	v_mul_f32_e32 v9, 0xbfb8aa3b, v145
	v_add_f32_e32 v6, 1.0, v6
	v_add_f32_e32 v7, 1.0, v7
	v_exp_f32_e32 v8, v8
	v_exp_f32_e32 v9, v9
	v_rcp_f32_e32 v6, v6
	v_rcp_f32_e32 v7, v7
	v_exp_f32_e32 v10, v10
	v_exp_f32_e32 v11, v11
	v_add_f32_e32 v8, 1.0, v8
	v_add_f32_e32 v9, 1.0, v9
	v_mul_f32_e32 v12, 0xbfb8aa3b, v136
	v_mul_f32_e32 v13, 0xbfb8aa3b, v137
	v_rcp_f32_e32 v8, v8
	v_rcp_f32_e32 v9, v9
	v_pk_mul_f32 v[6:7], v[142:143], v[6:7]
	v_add_f32_e32 v10, 1.0, v10
	v_add_f32_e32 v11, 1.0, v11
	v_exp_f32_e32 v12, v12
	v_exp_f32_e32 v13, v13
	v_pk_mul_f32 v[6:7], v[6:7], v[138:139]
	v_rcp_f32_e32 v10, v10
	v_rcp_f32_e32 v11, v11
	v_pk_mul_f32 v[6:7], v[6:7], s[66:67] op_sel_hi:[1,0]
	v_pk_mul_f32 v[8:9], v[144:145], v[8:9]
	v_med3_f32 v14, v6, s29, v1
	v_med3_f32 v7, v7, s29, v1
	v_mov_b32_e32 v6, v195
	v_add_f32_e32 v12, 1.0, v12
	v_add_f32_e32 v13, 1.0, v13
	v_cvt_pk_fp8_f32 v6, v14, v7
	v_pk_mul_f32 v[8:9], v[8:9], v[140:141]
	v_rcp_f32_e32 v12, v12
	v_rcp_f32_e32 v13, v13
	v_pk_mul_f32 v[10:11], v[134:135], v[10:11]
	v_pk_mul_f32 v[8:9], v[8:9], s[66:67] op_sel_hi:[1,0]
	v_pk_mul_f32 v[10:11], v[10:11], v[130:131]
	v_med3_f32 v7, v8, s29, v1
	v_pk_mul_f32 v[10:11], v[10:11], s[66:67] op_sel_hi:[1,0]
	v_med3_f32 v8, v9, s29, v1
	v_cvt_pk_fp8_f32 v6, v7, v8 op_sel:[0,0,1]
	v_med3_f32 v8, v10, s29, v1
	v_med3_f32 v9, v11, s29, v1
	v_mov_b32_e32 v7, v195
	v_pk_mul_f32 v[12:13], v[136:137], v[12:13]
	v_cvt_pk_fp8_f32 v7, v8, v9
	v_pk_mul_f32 v[12:13], v[12:13], v[132:133]
	v_or_b32_e32 v5, 48, v4
	v_pk_mul_f32 v[12:13], v[12:13], s[66:67] op_sel_hi:[1,0]
	v_mul_f32_e32 v10, 0xbfb8aa3b, v118
	v_med3_f32 v8, v12, s29, v1
	v_med3_f32 v9, v13, s29, v1
	v_cvt_pk_fp8_f32 v7, v8, v9 op_sel:[0,0,1]
	v_mad_i64_i32 v[8:9], s[38:39], v5, s2, v[2:3]
	v_mul_f32_e32 v11, 0xbfb8aa3b, v119
	global_store_dwordx2 v[8:9], v[6:7], off
	v_mul_f32_e32 v6, 0xbfb8aa3b, v126
	v_mul_f32_e32 v7, 0xbfb8aa3b, v127
	v_exp_f32_e32 v6, v6
	v_exp_f32_e32 v7, v7
	v_mul_f32_e32 v8, 0xbfb8aa3b, v128
	v_mul_f32_e32 v9, 0xbfb8aa3b, v129
	v_add_f32_e32 v6, 1.0, v6
	v_add_f32_e32 v7, 1.0, v7
	v_exp_f32_e32 v8, v8
	v_exp_f32_e32 v9, v9
	v_rcp_f32_e32 v6, v6
	v_rcp_f32_e32 v7, v7
	v_exp_f32_e32 v10, v10
	v_exp_f32_e32 v11, v11
	v_add_f32_e32 v8, 1.0, v8
	v_add_f32_e32 v9, 1.0, v9
	v_mul_f32_e32 v12, 0xbfb8aa3b, v120
	v_mul_f32_e32 v13, 0xbfb8aa3b, v121
	v_rcp_f32_e32 v8, v8
	v_rcp_f32_e32 v9, v9
	v_pk_mul_f32 v[6:7], v[126:127], v[6:7]
	v_add_f32_e32 v10, 1.0, v10
	v_add_f32_e32 v11, 1.0, v11
	v_exp_f32_e32 v12, v12
	v_exp_f32_e32 v13, v13
	v_pk_mul_f32 v[6:7], v[6:7], v[122:123]
	v_rcp_f32_e32 v10, v10
	v_rcp_f32_e32 v11, v11
	v_pk_mul_f32 v[6:7], v[6:7], s[66:67] op_sel_hi:[1,0]
	v_pk_mul_f32 v[8:9], v[128:129], v[8:9]
	v_med3_f32 v14, v6, s29, v1
	v_med3_f32 v7, v7, s29, v1
	v_mov_b32_e32 v6, v195
	v_add_f32_e32 v12, 1.0, v12
	v_add_f32_e32 v13, 1.0, v13
	v_cvt_pk_fp8_f32 v6, v14, v7
	v_pk_mul_f32 v[8:9], v[8:9], v[124:125]
	v_rcp_f32_e32 v12, v12
	v_rcp_f32_e32 v13, v13
	v_pk_mul_f32 v[10:11], v[118:119], v[10:11]
	v_pk_mul_f32 v[8:9], v[8:9], s[66:67] op_sel_hi:[1,0]
	v_pk_mul_f32 v[10:11], v[10:11], v[114:115]
	v_med3_f32 v7, v8, s29, v1
	v_pk_mul_f32 v[10:11], v[10:11], s[66:67] op_sel_hi:[1,0]
	v_med3_f32 v8, v9, s29, v1
	v_cvt_pk_fp8_f32 v6, v7, v8 op_sel:[0,0,1]
	v_med3_f32 v8, v10, s29, v1
	v_med3_f32 v9, v11, s29, v1
	v_mov_b32_e32 v7, v195
	v_pk_mul_f32 v[12:13], v[120:121], v[12:13]
	v_cvt_pk_fp8_f32 v7, v8, v9
	v_pk_mul_f32 v[12:13], v[12:13], v[116:117]
	v_add_u32_e32 v5, 0x80, v4
	v_pk_mul_f32 v[12:13], v[12:13], s[66:67] op_sel_hi:[1,0]
	v_mul_f32_e32 v10, 0xbfb8aa3b, v102
	v_med3_f32 v8, v12, s29, v1
	v_med3_f32 v9, v13, s29, v1
	v_cvt_pk_fp8_f32 v7, v8, v9 op_sel:[0,0,1]
	v_mad_i64_i32 v[8:9], s[38:39], v5, s2, v[2:3]
	v_mul_f32_e32 v11, 0xbfb8aa3b, v103
	global_store_dwordx2 v[8:9], v[6:7], off
	v_mul_f32_e32 v6, 0xbfb8aa3b, v110
	v_mul_f32_e32 v7, 0xbfb8aa3b, v111
	v_exp_f32_e32 v6, v6
	v_exp_f32_e32 v7, v7
	v_mul_f32_e32 v8, 0xbfb8aa3b, v112
	v_mul_f32_e32 v9, 0xbfb8aa3b, v113
	v_add_f32_e32 v6, 1.0, v6
	v_add_f32_e32 v7, 1.0, v7
	v_exp_f32_e32 v8, v8
	v_exp_f32_e32 v9, v9
	v_rcp_f32_e32 v6, v6
	v_rcp_f32_e32 v7, v7
	v_exp_f32_e32 v10, v10
	v_exp_f32_e32 v11, v11
	v_add_f32_e32 v8, 1.0, v8
	v_add_f32_e32 v9, 1.0, v9
	v_mul_f32_e32 v12, 0xbfb8aa3b, v104
	v_mul_f32_e32 v13, 0xbfb8aa3b, v105
	v_rcp_f32_e32 v8, v8
	v_rcp_f32_e32 v9, v9
	v_pk_mul_f32 v[6:7], v[110:111], v[6:7]
	v_add_f32_e32 v10, 1.0, v10
	v_add_f32_e32 v11, 1.0, v11
	v_exp_f32_e32 v12, v12
	v_exp_f32_e32 v13, v13
	v_pk_mul_f32 v[6:7], v[6:7], v[106:107]
	v_rcp_f32_e32 v10, v10
	v_rcp_f32_e32 v11, v11
	v_pk_mul_f32 v[6:7], v[6:7], s[66:67] op_sel_hi:[1,0]
	v_pk_mul_f32 v[8:9], v[112:113], v[8:9]
	v_med3_f32 v14, v6, s29, v1
	v_med3_f32 v7, v7, s29, v1
	v_mov_b32_e32 v6, v195
	v_add_f32_e32 v12, 1.0, v12
	v_add_f32_e32 v13, 1.0, v13
	v_cvt_pk_fp8_f32 v6, v14, v7
	v_pk_mul_f32 v[8:9], v[8:9], v[108:109]
	v_rcp_f32_e32 v12, v12
	v_rcp_f32_e32 v13, v13
	v_pk_mul_f32 v[10:11], v[102:103], v[10:11]
	v_pk_mul_f32 v[8:9], v[8:9], s[66:67] op_sel_hi:[1,0]
	v_pk_mul_f32 v[10:11], v[10:11], v[98:99]
	v_med3_f32 v7, v8, s29, v1
	v_pk_mul_f32 v[10:11], v[10:11], s[66:67] op_sel_hi:[1,0]
	v_med3_f32 v8, v9, s29, v1
	v_cvt_pk_fp8_f32 v6, v7, v8 op_sel:[0,0,1]
	v_med3_f32 v8, v10, s29, v1
	v_med3_f32 v9, v11, s29, v1
	v_mov_b32_e32 v7, v195
	v_pk_mul_f32 v[12:13], v[104:105], v[12:13]
	v_cvt_pk_fp8_f32 v7, v8, v9
	v_pk_mul_f32 v[12:13], v[12:13], v[100:101]
	v_add_u32_e32 v5, 0x90, v4
	v_pk_mul_f32 v[12:13], v[12:13], s[66:67] op_sel_hi:[1,0]
	v_mul_f32_e32 v10, 0xbfb8aa3b, v86
	v_med3_f32 v8, v12, s29, v1
	v_med3_f32 v9, v13, s29, v1
	v_cvt_pk_fp8_f32 v7, v8, v9 op_sel:[0,0,1]
	v_mad_i64_i32 v[8:9], s[38:39], v5, s2, v[2:3]
	v_mul_f32_e32 v11, 0xbfb8aa3b, v87
	global_store_dwordx2 v[8:9], v[6:7], off
	v_mul_f32_e32 v6, 0xbfb8aa3b, v94
	v_mul_f32_e32 v7, 0xbfb8aa3b, v95
	v_exp_f32_e32 v6, v6
	v_exp_f32_e32 v7, v7
	v_mul_f32_e32 v8, 0xbfb8aa3b, v96
	v_mul_f32_e32 v9, 0xbfb8aa3b, v97
	v_add_f32_e32 v6, 1.0, v6
	v_add_f32_e32 v7, 1.0, v7
	v_exp_f32_e32 v8, v8
	v_exp_f32_e32 v9, v9
	v_rcp_f32_e32 v6, v6
	v_rcp_f32_e32 v7, v7
	v_exp_f32_e32 v10, v10
	v_exp_f32_e32 v11, v11
	v_add_f32_e32 v8, 1.0, v8
	v_add_f32_e32 v9, 1.0, v9
	v_mul_f32_e32 v12, 0xbfb8aa3b, v88
	v_mul_f32_e32 v13, 0xbfb8aa3b, v89
	v_rcp_f32_e32 v8, v8
	v_rcp_f32_e32 v9, v9
	v_pk_mul_f32 v[6:7], v[94:95], v[6:7]
	v_add_f32_e32 v10, 1.0, v10
	v_add_f32_e32 v11, 1.0, v11
	v_exp_f32_e32 v12, v12
	v_exp_f32_e32 v13, v13
	v_pk_mul_f32 v[6:7], v[6:7], v[90:91]
	v_rcp_f32_e32 v10, v10
	v_rcp_f32_e32 v11, v11
	v_pk_mul_f32 v[6:7], v[6:7], s[66:67] op_sel_hi:[1,0]
	v_pk_mul_f32 v[8:9], v[96:97], v[8:9]
	v_med3_f32 v14, v6, s29, v1
	v_med3_f32 v7, v7, s29, v1
	v_mov_b32_e32 v6, v195
	v_add_f32_e32 v12, 1.0, v12
	v_add_f32_e32 v13, 1.0, v13
	v_cvt_pk_fp8_f32 v6, v14, v7
	v_pk_mul_f32 v[8:9], v[8:9], v[92:93]
	v_rcp_f32_e32 v12, v12
	v_rcp_f32_e32 v13, v13
	v_pk_mul_f32 v[10:11], v[86:87], v[10:11]
	v_pk_mul_f32 v[8:9], v[8:9], s[66:67] op_sel_hi:[1,0]
	v_pk_mul_f32 v[10:11], v[10:11], v[82:83]
	v_med3_f32 v7, v8, s29, v1
	v_pk_mul_f32 v[10:11], v[10:11], s[66:67] op_sel_hi:[1,0]
	v_med3_f32 v8, v9, s29, v1
	v_cvt_pk_fp8_f32 v6, v7, v8 op_sel:[0,0,1]
	v_med3_f32 v8, v10, s29, v1
	v_med3_f32 v9, v11, s29, v1
	v_mov_b32_e32 v7, v195
	v_pk_mul_f32 v[12:13], v[88:89], v[12:13]
	v_cvt_pk_fp8_f32 v7, v8, v9
	v_pk_mul_f32 v[12:13], v[12:13], v[84:85]
	v_add_u32_e32 v5, 0xa0, v4
	v_pk_mul_f32 v[12:13], v[12:13], s[66:67] op_sel_hi:[1,0]
	v_mul_f32_e32 v10, 0xbfb8aa3b, v72
	v_med3_f32 v8, v12, s29, v1
	v_med3_f32 v9, v13, s29, v1
	v_cvt_pk_fp8_f32 v7, v8, v9 op_sel:[0,0,1]
	v_mad_i64_i32 v[8:9], s[38:39], v5, s2, v[2:3]
	v_add_u32_e32 v12, 0xb0, v4
	v_mul_f32_e32 v4, 0xbfb8aa3b, v78
	v_mul_f32_e32 v5, 0xbfb8aa3b, v79
	v_exp_f32_e32 v4, v4
	v_exp_f32_e32 v5, v5
	global_store_dwordx2 v[8:9], v[6:7], off
	v_mul_f32_e32 v6, 0xbfb8aa3b, v80
	v_mul_f32_e32 v7, 0xbfb8aa3b, v81
	v_add_f32_e32 v4, 1.0, v4
	v_add_f32_e32 v5, 1.0, v5
	v_exp_f32_e32 v6, v6
	v_exp_f32_e32 v7, v7
	v_mul_f32_e32 v8, 0xbfb8aa3b, v70
	v_mul_f32_e32 v9, 0xbfb8aa3b, v71
	v_rcp_f32_e32 v4, v4
	v_rcp_f32_e32 v5, v5
	v_exp_f32_e32 v8, v8
	v_exp_f32_e32 v9, v9
	v_add_f32_e32 v6, 1.0, v6
	v_add_f32_e32 v7, 1.0, v7
	v_mul_f32_e32 v11, 0xbfb8aa3b, v73
	v_rcp_f32_e32 v6, v6
	v_rcp_f32_e32 v7, v7
	v_pk_mul_f32 v[4:5], v[78:79], v[4:5]
	v_add_f32_e32 v8, 1.0, v8
	v_add_f32_e32 v9, 1.0, v9
	v_exp_f32_e32 v10, v10
	v_exp_f32_e32 v11, v11
	v_pk_mul_f32 v[4:5], v[4:5], v[74:75]
	v_rcp_f32_e32 v8, v8
	v_rcp_f32_e32 v9, v9
	v_pk_mul_f32 v[4:5], v[4:5], s[66:67] op_sel_hi:[1,0]
	v_pk_mul_f32 v[6:7], v[80:81], v[6:7]
	v_med3_f32 v13, v4, s29, v1
	v_med3_f32 v5, v5, s29, v1
	v_mov_b32_e32 v4, v195
	v_add_f32_e32 v10, 1.0, v10
	v_add_f32_e32 v11, 1.0, v11
	v_cvt_pk_fp8_f32 v4, v13, v5
	v_pk_mul_f32 v[6:7], v[6:7], v[76:77]
	v_rcp_f32_e32 v10, v10
	v_rcp_f32_e32 v11, v11
	v_pk_mul_f32 v[8:9], v[70:71], v[8:9]
	v_pk_mul_f32 v[6:7], v[6:7], s[66:67] op_sel_hi:[1,0]
	v_pk_mul_f32 v[8:9], v[8:9], v[66:67]
	v_med3_f32 v5, v6, s29, v1
	v_pk_mul_f32 v[8:9], v[8:9], s[66:67] op_sel_hi:[1,0]
	v_med3_f32 v6, v7, s29, v1
	v_cvt_pk_fp8_f32 v4, v5, v6 op_sel:[0,0,1]
	v_med3_f32 v6, v8, s29, v1
	v_med3_f32 v7, v9, s29, v1
	v_mov_b32_e32 v5, v195
	v_pk_mul_f32 v[10:11], v[72:73], v[10:11]
	v_cvt_pk_fp8_f32 v5, v6, v7
	v_pk_mul_f32 v[10:11], v[10:11], v[68:69]
	v_mad_i64_i32 v[2:3], s[38:39], v12, s2, v[2:3]
	v_pk_mul_f32 v[10:11], v[10:11], s[66:67] op_sel_hi:[1,0]
	s_mov_b64 s[38:39], -1
	v_med3_f32 v6, v10, s29, v1
	v_med3_f32 v7, v11, s29, v1
	v_cvt_pk_fp8_f32 v5, v6, v7 op_sel:[0,0,1]
	global_store_dwordx2 v[2:3], v[4:5], off
	s_cbranch_vccnz .LBB0_1362
	s_andn2_b64 vcc, exec, s[80:81]
	s_cbranch_vccnz .LBB0_1361
	s_branch .LBB0_1361
